# copy item order: each wave copies consecutive k-blocks of one 32-column block, each XCD one contiguous eighth of a share (whole rows read, destination rows written contiguously)
# speedup vs baseline: 1.0082x; 1.0015x over previous
.Lmoe_site_T1:
	s_nop 1
	v_writelane_b32 v255, s0, 0
	v_writelane_b32 v255, s1, 1
	v_writelane_b32 v255, s2, 2
	v_writelane_b32 v255, s3, 3
	v_writelane_b32 v255, s4, 4
	v_writelane_b32 v255, s5, 5
	v_writelane_b32 v255, s6, 6
	v_writelane_b32 v255, s7, 7
	v_writelane_b32 v255, s8, 8
	v_writelane_b32 v255, s9, 9
	v_writelane_b32 v255, s10, 10
	v_writelane_b32 v255, s11, 11
	v_writelane_b32 v255, s12, 12
	v_writelane_b32 v255, s13, 13
	v_writelane_b32 v255, s14, 14
	v_writelane_b32 v255, s15, 15
	v_writelane_b32 v255, s16, 16
	v_writelane_b32 v255, s17, 17
	v_writelane_b32 v255, s18, 18
	v_writelane_b32 v255, s19, 19
	v_writelane_b32 v255, s20, 20
	v_writelane_b32 v255, s21, 21
	v_writelane_b32 v255, s22, 22
	v_writelane_b32 v255, s23, 23
	v_writelane_b32 v255, s24, 24
	v_writelane_b32 v255, s25, 25
	v_writelane_b32 v255, s26, 26
	v_writelane_b32 v255, s27, 27
	v_writelane_b32 v255, s28, 28
	v_writelane_b32 v255, s29, 29
	v_writelane_b32 v255, s30, 30
	v_writelane_b32 v255, s31, 31
	v_writelane_b32 v255, s32, 32
	v_writelane_b32 v255, s33, 33
	v_writelane_b32 v255, s34, 34
	v_writelane_b32 v255, s35, 35
	s_movk_i32 s0, 4
	v_readlane_b32 s20, v252, 32
	s_nop 3
	s_cmp_eq_u32 s20, 0
	s_cbranch_scc1 .Lmoe_T1_l1
	s_movk_i32 s2, 32
	s_movk_i32 s26, 1792
	s_mov_b32 s27, 0x1a00
	s_mov_b32 s28, 0x4000
	s_mov_b32 s29, 0x5e00
	s_mov_b32 s32, 0xbc00
	s_mov_b32 s33, 0x11a00
	s_mov_b32 s5, 0x4600
	s_mov_b32 s35, 0x0
	s_movk_i32 s34, 10
	s_branch .Lmoe_tail

.Lmoe_site_T2:
	s_nop 1
	v_writelane_b32 v255, s0, 0
	v_writelane_b32 v255, s1, 1
	v_writelane_b32 v255, s2, 2
	v_writelane_b32 v255, s3, 3
	v_writelane_b32 v255, s4, 4
	v_writelane_b32 v255, s5, 5
	v_writelane_b32 v255, s6, 6
	v_writelane_b32 v255, s7, 7
	v_writelane_b32 v255, s8, 8
	v_writelane_b32 v255, s9, 9
	v_writelane_b32 v255, s10, 10
	v_writelane_b32 v255, s11, 11
	v_writelane_b32 v255, s12, 12
	v_writelane_b32 v255, s13, 13
	v_writelane_b32 v255, s14, 14
	v_writelane_b32 v255, s15, 15
	v_writelane_b32 v255, s16, 16
	v_writelane_b32 v255, s17, 17
	v_writelane_b32 v255, s18, 18
	v_writelane_b32 v255, s19, 19
	v_writelane_b32 v255, s20, 20
	v_writelane_b32 v255, s21, 21
	v_writelane_b32 v255, s22, 22
	v_writelane_b32 v255, s23, 23
	v_writelane_b32 v255, s24, 24
	v_writelane_b32 v255, s25, 25
	v_writelane_b32 v255, s26, 26
	v_writelane_b32 v255, s27, 27
	v_writelane_b32 v255, s28, 28
	v_writelane_b32 v255, s29, 29
	v_writelane_b32 v255, s30, 30
	v_writelane_b32 v255, s31, 31
	v_writelane_b32 v255, s32, 32
	v_writelane_b32 v255, s33, 33
	v_writelane_b32 v255, s34, 34
	v_writelane_b32 v255, s35, 35
	s_movk_i32 s0, 5
	v_readlane_b32 s20, v252, 32
	s_nop 3
	s_cmp_eq_u32 s20, 0
	s_cbranch_scc1 .Lmoe_T2_l1
	s_movk_i32 s2, 128
	s_movk_i32 s26, 1024
	s_mov_b32 s27, 0x1800
	s_mov_b32 s28, 0x3e00
	s_mov_b32 s29, 0x1e000
	s_mov_b32 s32, 0x23e00
	s_mov_b32 s33, 0x29c00
	s_mov_b32 s5, 0x4000
	s_mov_b32 s35, 0x0
	s_movk_i32 s34, 16
	s_branch .Lmoe_tail

.Lmoe_site_T3:
	s_nop 1
	v_writelane_b32 v255, s0, 0
	v_writelane_b32 v255, s1, 1
	v_writelane_b32 v255, s2, 2
	v_writelane_b32 v255, s3, 3
	v_writelane_b32 v255, s4, 4
	v_writelane_b32 v255, s5, 5
	v_writelane_b32 v255, s6, 6
	v_writelane_b32 v255, s7, 7
	v_writelane_b32 v255, s8, 8
	v_writelane_b32 v255, s9, 9
	v_writelane_b32 v255, s10, 10
	v_writelane_b32 v255, s11, 11
	v_writelane_b32 v255, s12, 12
	v_writelane_b32 v255, s13, 13
	v_writelane_b32 v255, s14, 14
	v_writelane_b32 v255, s15, 15
	v_writelane_b32 v255, s16, 16
	v_writelane_b32 v255, s17, 17
	v_writelane_b32 v255, s18, 18
	v_writelane_b32 v255, s19, 19
	v_writelane_b32 v255, s20, 20
	v_writelane_b32 v255, s21, 21
	v_writelane_b32 v255, s22, 22
	v_writelane_b32 v255, s23, 23
	v_writelane_b32 v255, s24, 24
	v_writelane_b32 v255, s25, 25
	v_writelane_b32 v255, s26, 26
	v_writelane_b32 v255, s27, 27
	v_writelane_b32 v255, s28, 28
	v_writelane_b32 v255, s29, 29
	v_writelane_b32 v255, s30, 30
	v_writelane_b32 v255, s31, 31
	v_writelane_b32 v255, s32, 32
	v_writelane_b32 v255, s33, 33
	v_writelane_b32 v255, s34, 34
	v_writelane_b32 v255, s35, 35
	s_movk_i32 s0, 6
	v_readlane_b32 s20, v252, 32
	s_nop 3
	s_cmp_eq_u32 s20, 0
	s_cbranch_scc1 .Lmoe_T3_l1
	s_movk_i32 s2, 128
	s_movk_i32 s26, 1024
	s_mov_b32 s27, 0x1a00
	s_mov_b32 s28, 0x4000
	s_mov_b32 s29, 0x5e00
	s_mov_b32 s32, 0xbc00
	s_mov_b32 s33, 0x11a00
	s_mov_b32 s5, 0x6600
	s_mov_b32 s35, 0x4600
	s_movk_i32 s34, 8
	s_branch .Lmoe_tail
.Lmoe_T3_l1:
	s_movk_i32 s2, 64
	s_movk_i32 s26, 1536
	s_mov_b32 s27, 0x1800
	s_mov_b32 s28, 0x3e00
	s_mov_b32 s29, 0x1e000
	s_mov_b32 s32, 0x23e00
	s_mov_b32 s33, 0x29c00
	s_mov_b32 s5, 0x6400
	s_mov_b32 s35, 0x4000
	s_movk_i32 s34, 6
	s_branch .Lmoe_tail
.Lmoe_tail:
	s_mov_b64 s[30:31], exec
	s_mov_b64 exec, -1
	v_lshrrev_b32_e32 v16, 6, v0
	v_and_b32_e32 v17, 63, v0
	v_readlane_b32 s20, v252, 32
	v_readfirstlane_b32 s1, v16
	v_readlane_b32 s6, v253, 14
	v_readlane_b32 s7, v253, 15
	s_nop 3
	s_cmp_lt_u32 s90, s2
	s_cbranch_scc1 .Lmoe_exit
	s_sub_u32 s21, s90, s2
	s_lshl_b32 s21, s21, 3
	s_add_u32 s21, s21, s1
	s_and_b32 s22, s21, 63
	s_lshr_b32 s23, s21, 6
	s_mul_i32 s23, s23, s34
	s_lshl_b32 s23, s23, 6
	s_add_u32 s4, s35, s22
	s_add_u32 s4, s4, s23
	s_lshl_b32 s23, s34, 6
	s_add_u32 s5, s4, s23
	s_movk_i32 s26, 64
	s_branch .Lmoe_common
.Lmoe_p4:
	s_mov_b64 s[30:31], exec
	s_mov_b64 exec, -1
	v_lshrrev_b32_e32 v16, 6, v0
	v_and_b32_e32 v17, 63, v0
	v_readlane_b32 s20, v252, 32
	v_readfirstlane_b32 s1, v16
	v_readlane_b32 s6, v253, 14
	v_readlane_b32 s7, v253, 15
	s_nop 3
	s_cmp_eq_u32 s20, 0
	s_cselect_b32 s20, 0x18000, 0
	s_cselect_b32 s5, s34, s5
	s_sub_u32 s34, s5, s4
	s_lshr_b32 s34, s34, 9
	s_add_u32 s4, s4, s20
	s_and_b32 s21, s90, 7
	s_lshr_b32 s22, s90, 3
	s_lshl_b32 s21, s21, 3
	s_add_u32 s21, s21, s22
	s_sub_u32 s21, s21, s2
	s_lshl_b32 s21, s21, 3
	s_add_u32 s21, s21, s1
	s_and_b32 s22, s21, 63
	s_lshr_b32 s23, s21, 6
	s_mul_i32 s23, s23, s34
	s_lshl_b32 s23, s23, 6
	s_add_u32 s4, s4, s22
	s_add_u32 s4, s4, s23
	s_lshl_b32 s23, s34, 6
	s_add_u32 s5, s4, s23
	s_movk_i32 s26, 64
	s_mov_b32 s27, -1
	s_mov_b32 s28, -1
	s_mov_b32 s29, 0
	s_mov_b32 s32, 0
	s_mov_b32 s33, 0
